# t20
# baseline (speedup 1.0000x reference)
_Z11align_fusedPKfS0_PKiPf:
	s_load_dwordx8 s[4:11], s[0:1], 0x0
	s_sub_u32 s2, 0x1fff, s2
	s_mul_i32 s12, s2, 0x5dc0
	v_and_b32_e32 v7, 63, v0
	v_readfirstlane_b32 s13, v0
	v_lshlrev_b32_e32 v1, 4, v7
	v_mul_u32_u24_e32 v3, 12, v7
	s_mul_i32 s18, s13, 96
	s_mul_i32 s3, s13, 6
	s_sub_u32 s3, 0x49c, s3
	v_cmp_gt_u32_e64 s[14:15], s3, v7
	v_add_u32_e32 v2, s18, v1
	v_add_u32_e32 v3, s18, v3
	v_add_u32_e32 v4, 0x600, v3
	s_add_u32 s12, s12, s18
	s_add_u32 s12, s12, 0x800
	s_waitcnt lgkmcnt(0)
	s_sub_u32 s44, s12, 0x800
	s_add_u32 s40, s4, s44
	s_addc_u32 s41, s5, 0
	s_add_u32 s42, s40, 0x1000
	s_addc_u32 s43, s41, 0
	s_add_u32 s4, s4, s12
	s_addc_u32 s5, s5, 0
	s_add_u32 s10, s10, s12
	s_addc_u32 s11, s11, 0
	s_cmp_lg_u32 s13, 0
	s_cbranch_scc1 .Lbulk_waves
	v_lshlrev_b32_e32 v5, 2, v7
	global_load_dword v5, v5, s[8:9]
	global_load_dwordx3 v[44:46], v3, s[6:7] nt
	s_mov_b32 m0, s18
	s_nop 0
	global_load_lds_dwordx4 v1, s[40:41] nt
	global_load_lds_dwordx4 v1, s[40:41] offset:1024 nt
	global_load_lds_dwordx4 v1, s[40:41] offset:2048 nt
	global_load_lds_dwordx4 v1, s[40:41] offset:3072 nt
	s_add_u32 m0, s18, 0x1000
	s_nop 0
	global_load_lds_dwordx4 v1, s[42:43] nt
	global_load_lds_dwordx4 v1, s[42:43] offset:1024 nt
	s_mov_b32 s20, 0
	s_mov_b32 s21, 0x10000
	s_mov_b32 s22, 0
	s_mov_b32 s23, 0x20000
	s_mov_b32 s24, 0
	s_mov_b32 s25, 0x40000
	s_mov_b32 s26, 0
	s_mov_b32 s27, 0x80000
	s_waitcnt vmcnt(6)
	v_mul_u32_u24_e32 v5, 12, v5
	v_add_f32_dpp v52, v44, v44 quad_perm:[1,0,3,2] row_mask:0xf bank_mask:0xf
	v_add_f32_dpp v53, v45, v45 quad_perm:[1,0,3,2] row_mask:0xf bank_mask:0xf
	v_add_f32_dpp v54, v46, v46 quad_perm:[1,0,3,2] row_mask:0xf bank_mask:0xf
	v_add_f32_dpp v52, v52, v52 quad_perm:[2,3,0,1] row_mask:0xf bank_mask:0xf
	v_add_f32_dpp v53, v53, v53 quad_perm:[2,3,0,1] row_mask:0xf bank_mask:0xf
	v_add_f32_dpp v54, v54, v54 quad_perm:[2,3,0,1] row_mask:0xf bank_mask:0xf
	v_add_f32_dpp v52, v52, v52 row_half_mirror row_mask:0xf bank_mask:0xf
	v_add_f32_dpp v53, v53, v53 row_half_mirror row_mask:0xf bank_mask:0xf
	v_add_f32_dpp v54, v54, v54 row_half_mirror row_mask:0xf bank_mask:0xf
	v_add_f32_dpp v52, v52, v52 row_mirror row_mask:0xf bank_mask:0xf
	v_add_f32_dpp v53, v53, v53 row_mirror row_mask:0xf bank_mask:0xf
	v_add_f32_dpp v54, v54, v54 row_mirror row_mask:0xf bank_mask:0xf
	v_add_f32_dpp v52, v52, v52 row_bcast:15 row_mask:0xa bank_mask:0xf
	v_add_f32_dpp v53, v53, v53 row_bcast:15 row_mask:0xa bank_mask:0xf
	v_add_f32_dpp v54, v54, v54 row_bcast:15 row_mask:0xa bank_mask:0xf
	v_add_f32_dpp v52, v52, v52 row_bcast:31 row_mask:0xc bank_mask:0xf
	v_add_f32_dpp v53, v53, v53 row_bcast:31 row_mask:0xc bank_mask:0xf
	v_add_f32_dpp v54, v54, v54 row_bcast:31 row_mask:0xc bank_mask:0xf
	v_readlane_b32 s28, v52, 63
	v_readlane_b32 s29, v53, 63
	v_readlane_b32 s30, v54, 63
	v_mov_b32_e32 v52, s28
	v_mov_b32_e32 v53, s29
	v_mov_b32_e32 v54, s30
	v_fmac_f32_e32 v44, 0xbc800000, v52
	v_fmac_f32_e32 v45, 0xbc800000, v53
	v_fmac_f32_e32 v46, 0xbc800000, v54
	s_waitcnt vmcnt(0)
	s_waitcnt lgkmcnt(0)
	s_barrier
	ds_read2_b32 v[8:9], v3 offset0:0 offset1:1
	ds_read_b32 v24, v3 offset:8
	ds_read2_b32 v[10:11], v3 offset0:192 offset1:193
	ds_read_b32 v25, v3 offset:776
	ds_read2_b32 v[12:13], v4 offset0:0 offset1:1
	ds_read_b32 v26, v4 offset:8
	ds_read_b32 v48, v5
	ds_read_b32 v49, v5 offset:4
	ds_read_b32 v50, v5 offset:8
	s_waitcnt lgkmcnt(0)
	v_add_f32_dpp v52, v48, v48 quad_perm:[1,0,3,2] row_mask:0xf bank_mask:0xf
	v_add_f32_dpp v53, v49, v49 quad_perm:[1,0,3,2] row_mask:0xf bank_mask:0xf
	v_add_f32_dpp v54, v50, v50 quad_perm:[1,0,3,2] row_mask:0xf bank_mask:0xf
	v_add_f32_dpp v52, v52, v52 quad_perm:[2,3,0,1] row_mask:0xf bank_mask:0xf
	v_add_f32_dpp v53, v53, v53 quad_perm:[2,3,0,1] row_mask:0xf bank_mask:0xf
	v_add_f32_dpp v54, v54, v54 quad_perm:[2,3,0,1] row_mask:0xf bank_mask:0xf
	v_add_f32_dpp v52, v52, v52 row_half_mirror row_mask:0xf bank_mask:0xf
	v_add_f32_dpp v53, v53, v53 row_half_mirror row_mask:0xf bank_mask:0xf
	v_add_f32_dpp v54, v54, v54 row_half_mirror row_mask:0xf bank_mask:0xf
	v_add_f32_dpp v52, v52, v52 row_mirror row_mask:0xf bank_mask:0xf
	v_add_f32_dpp v53, v53, v53 row_mirror row_mask:0xf bank_mask:0xf
	v_add_f32_dpp v54, v54, v54 row_mirror row_mask:0xf bank_mask:0xf
	v_add_f32_dpp v52, v52, v52 row_bcast:15 row_mask:0xa bank_mask:0xf
	v_add_f32_dpp v53, v53, v53 row_bcast:15 row_mask:0xa bank_mask:0xf
	v_add_f32_dpp v54, v54, v54 row_bcast:15 row_mask:0xa bank_mask:0xf
	v_add_f32_dpp v52, v52, v52 row_bcast:31 row_mask:0xc bank_mask:0xf
	v_add_f32_dpp v53, v53, v53 row_bcast:31 row_mask:0xc bank_mask:0xf
	v_add_f32_dpp v54, v54, v54 row_bcast:31 row_mask:0xc bank_mask:0xf
	v_readlane_b32 s32, v52, 63
	v_readlane_b32 s33, v53, 63
	v_readlane_b32 s34, v54, 63
	v_mov_b32_e32 v52, s32
	v_mov_b32_e32 v53, s33
	v_mov_b32_e32 v54, s34
	v_fmac_f32_e32 v48, 0xbc800000, v52
	v_fmac_f32_e32 v49, 0xbc800000, v53
	v_fmac_f32_e32 v50, 0xbc800000, v54
	v_mul_f32_e32 v52, v48, v44
	v_mul_f32_e32 v53, v48, v45
	v_mul_f32_e32 v54, v48, v46
	v_mul_f32_e32 v55, v49, v44
	v_mul_f32_e32 v56, v49, v45
	v_mul_f32_e32 v57, v49, v46
	v_mul_f32_e32 v58, v50, v44
	v_mul_f32_e32 v59, v50, v45
	v_mul_f32_e32 v60, v50, v46
	v_add_f32_dpp v52, v52, v52 quad_perm:[1,0,3,2] row_mask:0xf bank_mask:0xf
	v_add_f32_dpp v53, v53, v53 quad_perm:[1,0,3,2] row_mask:0xf bank_mask:0xf
	v_add_f32_dpp v54, v54, v54 quad_perm:[1,0,3,2] row_mask:0xf bank_mask:0xf
	v_add_f32_dpp v55, v55, v55 quad_perm:[1,0,3,2] row_mask:0xf bank_mask:0xf
	v_add_f32_dpp v56, v56, v56 quad_perm:[1,0,3,2] row_mask:0xf bank_mask:0xf
	v_add_f32_dpp v57, v57, v57 quad_perm:[1,0,3,2] row_mask:0xf bank_mask:0xf
	v_add_f32_dpp v58, v58, v58 quad_perm:[1,0,3,2] row_mask:0xf bank_mask:0xf
	v_add_f32_dpp v59, v59, v59 quad_perm:[1,0,3,2] row_mask:0xf bank_mask:0xf
	v_add_f32_dpp v60, v60, v60 quad_perm:[1,0,3,2] row_mask:0xf bank_mask:0xf
	v_add_f32_dpp v52, v52, v52 quad_perm:[2,3,0,1] row_mask:0xf bank_mask:0xf
	v_add_f32_dpp v53, v53, v53 quad_perm:[2,3,0,1] row_mask:0xf bank_mask:0xf
	v_add_f32_dpp v54, v54, v54 quad_perm:[2,3,0,1] row_mask:0xf bank_mask:0xf
	v_add_f32_dpp v55, v55, v55 quad_perm:[2,3,0,1] row_mask:0xf bank_mask:0xf
	v_add_f32_dpp v56, v56, v56 quad_perm:[2,3,0,1] row_mask:0xf bank_mask:0xf
	v_add_f32_dpp v57, v57, v57 quad_perm:[2,3,0,1] row_mask:0xf bank_mask:0xf
	v_add_f32_dpp v58, v58, v58 quad_perm:[2,3,0,1] row_mask:0xf bank_mask:0xf
	v_add_f32_dpp v59, v59, v59 quad_perm:[2,3,0,1] row_mask:0xf bank_mask:0xf
	v_add_f32_dpp v60, v60, v60 quad_perm:[2,3,0,1] row_mask:0xf bank_mask:0xf
	v_add_f32_dpp v52, v52, v52 row_half_mirror row_mask:0xf bank_mask:0xf
	v_add_f32_dpp v53, v53, v53 row_half_mirror row_mask:0xf bank_mask:0xf
	v_add_f32_dpp v54, v54, v54 row_half_mirror row_mask:0xf bank_mask:0xf
	v_add_f32_dpp v55, v55, v55 row_half_mirror row_mask:0xf bank_mask:0xf
	v_add_f32_dpp v56, v56, v56 row_half_mirror row_mask:0xf bank_mask:0xf
	v_add_f32_dpp v57, v57, v57 row_half_mirror row_mask:0xf bank_mask:0xf
	v_add_f32_dpp v58, v58, v58 row_half_mirror row_mask:0xf bank_mask:0xf
	v_add_f32_dpp v59, v59, v59 row_half_mirror row_mask:0xf bank_mask:0xf
	v_add_f32_dpp v60, v60, v60 row_half_mirror row_mask:0xf bank_mask:0xf
	v_add_f32_dpp v52, v52, v52 row_mirror row_mask:0xf bank_mask:0xf
	v_add_f32_dpp v53, v53, v53 row_mirror row_mask:0xf bank_mask:0xf
	v_add_f32_dpp v54, v54, v54 row_mirror row_mask:0xf bank_mask:0xf
	v_add_f32_dpp v55, v55, v55 row_mirror row_mask:0xf bank_mask:0xf
	v_add_f32_dpp v56, v56, v56 row_mirror row_mask:0xf bank_mask:0xf
	v_add_f32_dpp v57, v57, v57 row_mirror row_mask:0xf bank_mask:0xf
	v_add_f32_dpp v58, v58, v58 row_mirror row_mask:0xf bank_mask:0xf
	v_add_f32_dpp v59, v59, v59 row_mirror row_mask:0xf bank_mask:0xf
	v_add_f32_dpp v60, v60, v60 row_mirror row_mask:0xf bank_mask:0xf
	v_add_f32_dpp v52, v52, v52 row_bcast:15 row_mask:0xa bank_mask:0xf
	v_add_f32_dpp v53, v53, v53 row_bcast:15 row_mask:0xa bank_mask:0xf
	v_add_f32_dpp v54, v54, v54 row_bcast:15 row_mask:0xa bank_mask:0xf
	v_add_f32_dpp v55, v55, v55 row_bcast:15 row_mask:0xa bank_mask:0xf
	v_add_f32_dpp v56, v56, v56 row_bcast:15 row_mask:0xa bank_mask:0xf
	v_add_f32_dpp v57, v57, v57 row_bcast:15 row_mask:0xa bank_mask:0xf
	v_add_f32_dpp v58, v58, v58 row_bcast:15 row_mask:0xa bank_mask:0xf
	v_add_f32_dpp v59, v59, v59 row_bcast:15 row_mask:0xa bank_mask:0xf
	v_add_f32_dpp v60, v60, v60 row_bcast:15 row_mask:0xa bank_mask:0xf
	v_add_f32_dpp v52, v52, v52 row_bcast:31 row_mask:0xc bank_mask:0xf
	v_add_f32_dpp v53, v53, v53 row_bcast:31 row_mask:0xc bank_mask:0xf
	v_add_f32_dpp v54, v54, v54 row_bcast:31 row_mask:0xc bank_mask:0xf
	v_add_f32_dpp v55, v55, v55 row_bcast:31 row_mask:0xc bank_mask:0xf
	v_add_f32_dpp v56, v56, v56 row_bcast:31 row_mask:0xc bank_mask:0xf
	v_add_f32_dpp v57, v57, v57 row_bcast:31 row_mask:0xc bank_mask:0xf
	v_add_f32_dpp v58, v58, v58 row_bcast:31 row_mask:0xc bank_mask:0xf
	v_add_f32_dpp v59, v59, v59 row_bcast:31 row_mask:0xc bank_mask:0xf
	v_add_f32_dpp v60, v60, v60 row_bcast:31 row_mask:0xc bank_mask:0xf
	v_cndmask_b32_e64 v52, v52, v55, s[22:23]
	v_cndmask_b32_e64 v53, v53, v56, s[22:23]
	v_cndmask_b32_e64 v54, v54, v57, s[22:23]
	v_cndmask_b32_e64 v52, v52, v58, s[24:25]
	v_cndmask_b32_e64 v53, v53, v59, s[24:25]
	v_cndmask_b32_e64 v54, v54, v60, s[24:25]
	v_cndmask_b32_e64 v52, v52, 0, s[26:27]
	v_cndmask_b32_e64 v53, v53, 0, s[26:27]
	v_cndmask_b32_e64 v54, v54, 0, s[26:27]
	v_cndmask_b32_e64 v40, 0, 1.0, s[20:21]
	v_cndmask_b32_e64 v41, 0, 1.0, s[22:23]
	v_cndmask_b32_e64 v42, 0, 1.0, s[24:25]
	v_mul_f32_e32 v55, v52, v52
	v_mul_f32_e32 v56, v53, v53
	v_mul_f32_e32 v57, v52, v53
	v_add_f32_dpp v55, v55, v55 quad_perm:[1,0,3,2] row_mask:0xf bank_mask:0xf
	v_add_f32_dpp v56, v56, v56 quad_perm:[1,0,3,2] row_mask:0xf bank_mask:0xf
	v_add_f32_dpp v57, v57, v57 quad_perm:[1,0,3,2] row_mask:0xf bank_mask:0xf
	v_add_f32_dpp v55, v55, v55 quad_perm:[2,3,0,1] row_mask:0xf bank_mask:0xf
	v_add_f32_dpp v56, v56, v56 quad_perm:[2,3,0,1] row_mask:0xf bank_mask:0xf
	v_add_f32_dpp v57, v57, v57 quad_perm:[2,3,0,1] row_mask:0xf bank_mask:0xf
	v_sub_f32_e32 v60, v56, v55
	v_mul_f32_e32 v58, v57, v57
	v_cmp_gt_f32_e32 vcc, 0, v60
	v_mul_f32_e32 v59, v60, v60
	v_fmac_f32_e32 v59, 4.0, v58
	v_sqrt_f32_e32 v59, v59
	s_nop 0
	v_add_f32_e64 v59, |v60|, v59
	v_add_f32_e32 v59, 0x0da24260, v59
	v_rcp_f32_e32 v59, v59
	v_add_f32_e32 v58, v57, v57
	v_mul_f32_e32 v59, v58, v59
	v_cndmask_b32_e64 v59, v59, -v59, vcc
	v_fma_f32 v58, v59, v59, 1.0
	v_rsq_f32_e32 v61, v58
	s_nop 0
	v_mul_f32_e32 v62, v61, v59
	v_mul_f32_e32 v55, v62, v53
	v_mul_f32_e32 v56, v62, v52
	v_fma_f32 v52, v61, v52, -v55
	v_fma_f32 v53, v61, v53, v56
	v_mul_f32_e32 v55, v52, v52
	v_mul_f32_e32 v56, v54, v54
	v_mul_f32_e32 v57, v52, v54
	v_add_f32_dpp v55, v55, v55 quad_perm:[1,0,3,2] row_mask:0xf bank_mask:0xf
	v_add_f32_dpp v56, v56, v56 quad_perm:[1,0,3,2] row_mask:0xf bank_mask:0xf
	v_add_f32_dpp v57, v57, v57 quad_perm:[1,0,3,2] row_mask:0xf bank_mask:0xf
	v_add_f32_dpp v55, v55, v55 quad_perm:[2,3,0,1] row_mask:0xf bank_mask:0xf
	v_add_f32_dpp v56, v56, v56 quad_perm:[2,3,0,1] row_mask:0xf bank_mask:0xf
	v_add_f32_dpp v57, v57, v57 quad_perm:[2,3,0,1] row_mask:0xf bank_mask:0xf
	v_sub_f32_e32 v60, v56, v55
	v_mul_f32_e32 v58, v57, v57
	v_cmp_gt_f32_e32 vcc, 0, v60
	v_mul_f32_e32 v59, v60, v60
	v_fmac_f32_e32 v59, 4.0, v58
	v_sqrt_f32_e32 v59, v59
	v_mul_f32_e32 v63, v62, v41
	v_mul_f32_e32 v43, v62, v40
	v_fma_f32 v40, v61, v40, -v63
	v_fma_f32 v41, v61, v41, v43
	v_add_f32_e64 v59, |v60|, v59
	v_add_f32_e32 v59, 0x0da24260, v59
	v_rcp_f32_e32 v59, v59
	v_add_f32_e32 v58, v57, v57
	v_mul_f32_e32 v59, v58, v59
	v_cndmask_b32_e64 v59, v59, -v59, vcc
	v_fma_f32 v58, v59, v59, 1.0
	v_rsq_f32_e32 v61, v58
	s_nop 0
	v_mul_f32_e32 v62, v61, v59
	v_mul_f32_e32 v55, v62, v54
	v_mul_f32_e32 v56, v62, v52
	v_fma_f32 v52, v61, v52, -v55
	v_fma_f32 v54, v61, v54, v56
	v_mul_f32_e32 v55, v53, v53
	v_mul_f32_e32 v56, v54, v54
	v_mul_f32_e32 v57, v53, v54
	v_add_f32_dpp v55, v55, v55 quad_perm:[1,0,3,2] row_mask:0xf bank_mask:0xf
	v_add_f32_dpp v56, v56, v56 quad_perm:[1,0,3,2] row_mask:0xf bank_mask:0xf
	v_add_f32_dpp v57, v57, v57 quad_perm:[1,0,3,2] row_mask:0xf bank_mask:0xf
	v_add_f32_dpp v55, v55, v55 quad_perm:[2,3,0,1] row_mask:0xf bank_mask:0xf
	v_add_f32_dpp v56, v56, v56 quad_perm:[2,3,0,1] row_mask:0xf bank_mask:0xf
	v_add_f32_dpp v57, v57, v57 quad_perm:[2,3,0,1] row_mask:0xf bank_mask:0xf
	v_sub_f32_e32 v60, v56, v55
	v_mul_f32_e32 v58, v57, v57
	v_cmp_gt_f32_e32 vcc, 0, v60
	v_mul_f32_e32 v59, v60, v60
	v_fmac_f32_e32 v59, 4.0, v58
	v_sqrt_f32_e32 v59, v59
	v_mul_f32_e32 v63, v62, v42
	v_mul_f32_e32 v43, v62, v40
	v_fma_f32 v40, v61, v40, -v63
	v_fma_f32 v42, v61, v42, v43
	v_add_f32_e64 v59, |v60|, v59
	v_add_f32_e32 v59, 0x0da24260, v59
	v_rcp_f32_e32 v59, v59
	v_add_f32_e32 v58, v57, v57
	v_mul_f32_e32 v59, v58, v59
	v_cndmask_b32_e64 v59, v59, -v59, vcc
	v_fma_f32 v58, v59, v59, 1.0
	v_rsq_f32_e32 v61, v58
	s_nop 0
	v_mul_f32_e32 v62, v61, v59
	v_mul_f32_e32 v55, v62, v54
	v_mul_f32_e32 v56, v62, v53
	v_fma_f32 v53, v61, v53, -v55
	v_fma_f32 v54, v61, v54, v56
	v_mul_f32_e32 v55, v52, v52
	v_mul_f32_e32 v56, v53, v53
	v_mul_f32_e32 v57, v52, v53
	v_add_f32_dpp v55, v55, v55 quad_perm:[1,0,3,2] row_mask:0xf bank_mask:0xf
	v_add_f32_dpp v56, v56, v56 quad_perm:[1,0,3,2] row_mask:0xf bank_mask:0xf
	v_add_f32_dpp v57, v57, v57 quad_perm:[1,0,3,2] row_mask:0xf bank_mask:0xf
	v_add_f32_dpp v55, v55, v55 quad_perm:[2,3,0,1] row_mask:0xf bank_mask:0xf
	v_add_f32_dpp v56, v56, v56 quad_perm:[2,3,0,1] row_mask:0xf bank_mask:0xf
	v_add_f32_dpp v57, v57, v57 quad_perm:[2,3,0,1] row_mask:0xf bank_mask:0xf
	v_sub_f32_e32 v60, v56, v55
	v_mul_f32_e32 v58, v57, v57
	v_cmp_gt_f32_e32 vcc, 0, v60
	v_mul_f32_e32 v59, v60, v60
	v_fmac_f32_e32 v59, 4.0, v58
	v_sqrt_f32_e32 v59, v59
	v_mul_f32_e32 v63, v62, v42
	v_mul_f32_e32 v43, v62, v41
	v_fma_f32 v41, v61, v41, -v63
	v_fma_f32 v42, v61, v42, v43
	v_add_f32_e64 v59, |v60|, v59
	v_add_f32_e32 v59, 0x0da24260, v59
	v_rcp_f32_e32 v59, v59
	v_add_f32_e32 v58, v57, v57
	v_mul_f32_e32 v59, v58, v59
	v_cndmask_b32_e64 v59, v59, -v59, vcc
	v_fma_f32 v58, v59, v59, 1.0
	v_rsq_f32_e32 v61, v58
	s_nop 0
	v_mul_f32_e32 v62, v61, v59
	v_mul_f32_e32 v55, v62, v53
	v_mul_f32_e32 v56, v62, v52
	v_fma_f32 v52, v61, v52, -v55
	v_fma_f32 v53, v61, v53, v56
	v_mul_f32_e32 v55, v52, v52
	v_mul_f32_e32 v56, v54, v54
	v_mul_f32_e32 v57, v52, v54
	v_add_f32_dpp v55, v55, v55 quad_perm:[1,0,3,2] row_mask:0xf bank_mask:0xf
	v_add_f32_dpp v56, v56, v56 quad_perm:[1,0,3,2] row_mask:0xf bank_mask:0xf
	v_add_f32_dpp v57, v57, v57 quad_perm:[1,0,3,2] row_mask:0xf bank_mask:0xf
	v_add_f32_dpp v55, v55, v55 quad_perm:[2,3,0,1] row_mask:0xf bank_mask:0xf
	v_add_f32_dpp v56, v56, v56 quad_perm:[2,3,0,1] row_mask:0xf bank_mask:0xf
	v_add_f32_dpp v57, v57, v57 quad_perm:[2,3,0,1] row_mask:0xf bank_mask:0xf
	v_sub_f32_e32 v60, v56, v55
	v_mul_f32_e32 v58, v57, v57
	v_cmp_gt_f32_e32 vcc, 0, v60
	v_mul_f32_e32 v59, v60, v60
	v_fmac_f32_e32 v59, 4.0, v58
	v_sqrt_f32_e32 v59, v59
	v_mul_f32_e32 v63, v62, v41
	v_mul_f32_e32 v43, v62, v40
	v_fma_f32 v40, v61, v40, -v63
	v_fma_f32 v41, v61, v41, v43
	v_add_f32_e64 v59, |v60|, v59
	v_add_f32_e32 v59, 0x0da24260, v59
	v_rcp_f32_e32 v59, v59
	v_add_f32_e32 v58, v57, v57
	v_mul_f32_e32 v59, v58, v59
	v_cndmask_b32_e64 v59, v59, -v59, vcc
	v_fma_f32 v58, v59, v59, 1.0
	v_rsq_f32_e32 v61, v58
	s_nop 0
	v_mul_f32_e32 v62, v61, v59
	v_mul_f32_e32 v55, v62, v54
	v_mul_f32_e32 v56, v62, v52
	v_fma_f32 v52, v61, v52, -v55
	v_fma_f32 v54, v61, v54, v56
	v_mul_f32_e32 v55, v53, v53
	v_mul_f32_e32 v56, v54, v54
	v_mul_f32_e32 v57, v53, v54
	v_add_f32_dpp v55, v55, v55 quad_perm:[1,0,3,2] row_mask:0xf bank_mask:0xf
	v_add_f32_dpp v56, v56, v56 quad_perm:[1,0,3,2] row_mask:0xf bank_mask:0xf
	v_add_f32_dpp v57, v57, v57 quad_perm:[1,0,3,2] row_mask:0xf bank_mask:0xf
	v_add_f32_dpp v55, v55, v55 quad_perm:[2,3,0,1] row_mask:0xf bank_mask:0xf
	v_add_f32_dpp v56, v56, v56 quad_perm:[2,3,0,1] row_mask:0xf bank_mask:0xf
	v_add_f32_dpp v57, v57, v57 quad_perm:[2,3,0,1] row_mask:0xf bank_mask:0xf
	v_sub_f32_e32 v60, v56, v55
	v_mul_f32_e32 v58, v57, v57
	v_cmp_gt_f32_e32 vcc, 0, v60
	v_mul_f32_e32 v59, v60, v60
	v_fmac_f32_e32 v59, 4.0, v58
	v_sqrt_f32_e32 v59, v59
	v_mul_f32_e32 v63, v62, v42
	v_mul_f32_e32 v43, v62, v40
	v_fma_f32 v40, v61, v40, -v63
	v_fma_f32 v42, v61, v42, v43
	v_add_f32_e64 v59, |v60|, v59
	v_add_f32_e32 v59, 0x0da24260, v59
	v_rcp_f32_e32 v59, v59
	v_add_f32_e32 v58, v57, v57
	v_mul_f32_e32 v59, v58, v59
	v_cndmask_b32_e64 v59, v59, -v59, vcc
	v_fma_f32 v58, v59, v59, 1.0
	v_rsq_f32_e32 v61, v58
	s_nop 0
	v_mul_f32_e32 v62, v61, v59
	v_mul_f32_e32 v55, v62, v54
	v_mul_f32_e32 v56, v62, v53
	v_fma_f32 v53, v61, v53, -v55
	v_fma_f32 v54, v61, v54, v56
	v_mul_f32_e32 v55, v52, v52
	v_mul_f32_e32 v56, v53, v53
	v_mul_f32_e32 v57, v52, v53
	v_add_f32_dpp v55, v55, v55 quad_perm:[1,0,3,2] row_mask:0xf bank_mask:0xf
	v_add_f32_dpp v56, v56, v56 quad_perm:[1,0,3,2] row_mask:0xf bank_mask:0xf
	v_add_f32_dpp v57, v57, v57 quad_perm:[1,0,3,2] row_mask:0xf bank_mask:0xf
	v_add_f32_dpp v55, v55, v55 quad_perm:[2,3,0,1] row_mask:0xf bank_mask:0xf
	v_add_f32_dpp v56, v56, v56 quad_perm:[2,3,0,1] row_mask:0xf bank_mask:0xf
	v_add_f32_dpp v57, v57, v57 quad_perm:[2,3,0,1] row_mask:0xf bank_mask:0xf
	v_sub_f32_e32 v60, v56, v55
	v_mul_f32_e32 v58, v57, v57
	v_cmp_gt_f32_e32 vcc, 0, v60
	v_mul_f32_e32 v59, v60, v60
	v_fmac_f32_e32 v59, 4.0, v58
	v_sqrt_f32_e32 v59, v59
	v_mul_f32_e32 v63, v62, v42
	v_mul_f32_e32 v43, v62, v41
	v_fma_f32 v41, v61, v41, -v63
	v_fma_f32 v42, v61, v42, v43
	v_add_f32_e64 v59, |v60|, v59
	v_add_f32_e32 v59, 0x0da24260, v59
	v_rcp_f32_e32 v59, v59
	v_add_f32_e32 v58, v57, v57
	v_mul_f32_e32 v59, v58, v59
	v_cndmask_b32_e64 v59, v59, -v59, vcc
	v_fma_f32 v58, v59, v59, 1.0
	v_rsq_f32_e32 v61, v58
	s_nop 0
	v_mul_f32_e32 v62, v61, v59
	v_mul_f32_e32 v55, v62, v53
	v_mul_f32_e32 v56, v62, v52
	v_fma_f32 v52, v61, v52, -v55
	v_fma_f32 v53, v61, v53, v56
	v_mul_f32_e32 v55, v52, v52
	v_mul_f32_e32 v56, v54, v54
	v_mul_f32_e32 v57, v52, v54
	v_add_f32_dpp v55, v55, v55 quad_perm:[1,0,3,2] row_mask:0xf bank_mask:0xf
	v_add_f32_dpp v56, v56, v56 quad_perm:[1,0,3,2] row_mask:0xf bank_mask:0xf
	v_add_f32_dpp v57, v57, v57 quad_perm:[1,0,3,2] row_mask:0xf bank_mask:0xf
	v_add_f32_dpp v55, v55, v55 quad_perm:[2,3,0,1] row_mask:0xf bank_mask:0xf
	v_add_f32_dpp v56, v56, v56 quad_perm:[2,3,0,1] row_mask:0xf bank_mask:0xf
	v_add_f32_dpp v57, v57, v57 quad_perm:[2,3,0,1] row_mask:0xf bank_mask:0xf
	v_sub_f32_e32 v60, v56, v55
	v_mul_f32_e32 v58, v57, v57
	v_cmp_gt_f32_e32 vcc, 0, v60
	v_mul_f32_e32 v59, v60, v60
	v_fmac_f32_e32 v59, 4.0, v58
	v_sqrt_f32_e32 v59, v59
	v_mul_f32_e32 v63, v62, v41
	v_mul_f32_e32 v43, v62, v40
	v_fma_f32 v40, v61, v40, -v63
	v_fma_f32 v41, v61, v41, v43
	v_add_f32_e64 v59, |v60|, v59
	v_add_f32_e32 v59, 0x0da24260, v59
	v_rcp_f32_e32 v59, v59
	v_add_f32_e32 v58, v57, v57
	v_mul_f32_e32 v59, v58, v59
	v_cndmask_b32_e64 v59, v59, -v59, vcc
	v_fma_f32 v58, v59, v59, 1.0
	v_rsq_f32_e32 v61, v58
	s_nop 0
	v_mul_f32_e32 v62, v61, v59
	v_mul_f32_e32 v55, v62, v54
	v_mul_f32_e32 v56, v62, v52
	v_fma_f32 v52, v61, v52, -v55
	v_fma_f32 v54, v61, v54, v56
	v_mul_f32_e32 v55, v53, v53
	v_mul_f32_e32 v56, v54, v54
	v_mul_f32_e32 v57, v53, v54
	v_add_f32_dpp v55, v55, v55 quad_perm:[1,0,3,2] row_mask:0xf bank_mask:0xf
	v_add_f32_dpp v56, v56, v56 quad_perm:[1,0,3,2] row_mask:0xf bank_mask:0xf
	v_add_f32_dpp v57, v57, v57 quad_perm:[1,0,3,2] row_mask:0xf bank_mask:0xf
	v_add_f32_dpp v55, v55, v55 quad_perm:[2,3,0,1] row_mask:0xf bank_mask:0xf
	v_add_f32_dpp v56, v56, v56 quad_perm:[2,3,0,1] row_mask:0xf bank_mask:0xf
	v_add_f32_dpp v57, v57, v57 quad_perm:[2,3,0,1] row_mask:0xf bank_mask:0xf
	v_sub_f32_e32 v60, v56, v55
	v_mul_f32_e32 v58, v57, v57
	v_cmp_gt_f32_e32 vcc, 0, v60
	v_mul_f32_e32 v59, v60, v60
	v_fmac_f32_e32 v59, 4.0, v58
	v_sqrt_f32_e32 v59, v59
	v_mul_f32_e32 v63, v62, v42
	v_mul_f32_e32 v43, v62, v40
	v_fma_f32 v40, v61, v40, -v63
	v_fma_f32 v42, v61, v42, v43
	v_add_f32_e64 v59, |v60|, v59
	v_add_f32_e32 v59, 0x0da24260, v59
	v_rcp_f32_e32 v59, v59
	v_add_f32_e32 v58, v57, v57
	v_mul_f32_e32 v59, v58, v59
	v_cndmask_b32_e64 v59, v59, -v59, vcc
	v_fma_f32 v58, v59, v59, 1.0
	v_rsq_f32_e32 v61, v58
	s_nop 0
	v_mul_f32_e32 v62, v61, v59
	v_mul_f32_e32 v55, v62, v54
	v_mul_f32_e32 v56, v62, v53
	v_fma_f32 v53, v61, v53, -v55
	v_fma_f32 v54, v61, v54, v56
	v_mul_f32_e32 v55, v52, v52
	v_mul_f32_e32 v56, v53, v53
	v_mul_f32_e32 v57, v52, v53
	v_add_f32_dpp v55, v55, v55 quad_perm:[1,0,3,2] row_mask:0xf bank_mask:0xf
	v_add_f32_dpp v56, v56, v56 quad_perm:[1,0,3,2] row_mask:0xf bank_mask:0xf
	v_add_f32_dpp v57, v57, v57 quad_perm:[1,0,3,2] row_mask:0xf bank_mask:0xf
	v_add_f32_dpp v55, v55, v55 quad_perm:[2,3,0,1] row_mask:0xf bank_mask:0xf
	v_add_f32_dpp v56, v56, v56 quad_perm:[2,3,0,1] row_mask:0xf bank_mask:0xf
	v_add_f32_dpp v57, v57, v57 quad_perm:[2,3,0,1] row_mask:0xf bank_mask:0xf
	v_sub_f32_e32 v60, v56, v55
	v_mul_f32_e32 v58, v57, v57
	v_cmp_gt_f32_e32 vcc, 0, v60
	v_mul_f32_e32 v59, v60, v60
	v_fmac_f32_e32 v59, 4.0, v58
	v_sqrt_f32_e32 v59, v59
	v_mul_f32_e32 v63, v62, v42
	v_mul_f32_e32 v43, v62, v41
	v_fma_f32 v41, v61, v41, -v63
	v_fma_f32 v42, v61, v42, v43
	v_add_f32_e64 v59, |v60|, v59
	v_add_f32_e32 v59, 0x0da24260, v59
	v_rcp_f32_e32 v59, v59
	v_add_f32_e32 v58, v57, v57
	v_mul_f32_e32 v59, v58, v59
	v_cndmask_b32_e64 v59, v59, -v59, vcc
	v_fma_f32 v58, v59, v59, 1.0
	v_rsq_f32_e32 v61, v58
	s_nop 0
	v_mul_f32_e32 v62, v61, v59
	v_mul_f32_e32 v55, v62, v53
	v_mul_f32_e32 v56, v62, v52
	v_fma_f32 v52, v61, v52, -v55
	v_fma_f32 v53, v61, v53, v56
	v_mul_f32_e32 v55, v52, v52
	v_mul_f32_e32 v56, v54, v54
	v_mul_f32_e32 v57, v52, v54
	v_add_f32_dpp v55, v55, v55 quad_perm:[1,0,3,2] row_mask:0xf bank_mask:0xf
	v_add_f32_dpp v56, v56, v56 quad_perm:[1,0,3,2] row_mask:0xf bank_mask:0xf
	v_add_f32_dpp v57, v57, v57 quad_perm:[1,0,3,2] row_mask:0xf bank_mask:0xf
	v_add_f32_dpp v55, v55, v55 quad_perm:[2,3,0,1] row_mask:0xf bank_mask:0xf
	v_add_f32_dpp v56, v56, v56 quad_perm:[2,3,0,1] row_mask:0xf bank_mask:0xf
	v_add_f32_dpp v57, v57, v57 quad_perm:[2,3,0,1] row_mask:0xf bank_mask:0xf
	v_sub_f32_e32 v60, v56, v55
	v_mul_f32_e32 v58, v57, v57
	v_cmp_gt_f32_e32 vcc, 0, v60
	v_mul_f32_e32 v59, v60, v60
	v_fmac_f32_e32 v59, 4.0, v58
	v_sqrt_f32_e32 v59, v59
	v_mul_f32_e32 v63, v62, v41
	v_mul_f32_e32 v43, v62, v40
	v_fma_f32 v40, v61, v40, -v63
	v_fma_f32 v41, v61, v41, v43
	v_add_f32_e64 v59, |v60|, v59
	v_add_f32_e32 v59, 0x0da24260, v59
	v_rcp_f32_e32 v59, v59
	v_add_f32_e32 v58, v57, v57
	v_mul_f32_e32 v59, v58, v59
	v_cndmask_b32_e64 v59, v59, -v59, vcc
	v_fma_f32 v58, v59, v59, 1.0
	v_rsq_f32_e32 v61, v58
	s_nop 0
	v_mul_f32_e32 v62, v61, v59
	v_mul_f32_e32 v55, v62, v54
	v_mul_f32_e32 v56, v62, v52
	v_fma_f32 v52, v61, v52, -v55
	v_fma_f32 v54, v61, v54, v56
	v_mul_f32_e32 v55, v53, v53
	v_mul_f32_e32 v56, v54, v54
	v_mul_f32_e32 v57, v53, v54
	v_add_f32_dpp v55, v55, v55 quad_perm:[1,0,3,2] row_mask:0xf bank_mask:0xf
	v_add_f32_dpp v56, v56, v56 quad_perm:[1,0,3,2] row_mask:0xf bank_mask:0xf
	v_add_f32_dpp v57, v57, v57 quad_perm:[1,0,3,2] row_mask:0xf bank_mask:0xf
	v_add_f32_dpp v55, v55, v55 quad_perm:[2,3,0,1] row_mask:0xf bank_mask:0xf
	v_add_f32_dpp v56, v56, v56 quad_perm:[2,3,0,1] row_mask:0xf bank_mask:0xf
	v_add_f32_dpp v57, v57, v57 quad_perm:[2,3,0,1] row_mask:0xf bank_mask:0xf
	v_sub_f32_e32 v60, v56, v55
	v_mul_f32_e32 v58, v57, v57
	v_cmp_gt_f32_e32 vcc, 0, v60
	v_mul_f32_e32 v59, v60, v60
	v_fmac_f32_e32 v59, 4.0, v58
	v_sqrt_f32_e32 v59, v59
	v_mul_f32_e32 v63, v62, v42
	v_mul_f32_e32 v43, v62, v40
	v_fma_f32 v40, v61, v40, -v63
	v_fma_f32 v42, v61, v42, v43
	v_add_f32_e64 v59, |v60|, v59
	v_add_f32_e32 v59, 0x0da24260, v59
	v_rcp_f32_e32 v59, v59
	v_add_f32_e32 v58, v57, v57
	v_mul_f32_e32 v59, v58, v59
	v_cndmask_b32_e64 v59, v59, -v59, vcc
	v_fma_f32 v58, v59, v59, 1.0
	v_rsq_f32_e32 v61, v58
	s_nop 0
	v_mul_f32_e32 v62, v61, v59
	v_mul_f32_e32 v55, v62, v54
	v_mul_f32_e32 v56, v62, v53
	v_fma_f32 v53, v61, v53, -v55
	v_fma_f32 v54, v61, v54, v56
	v_mul_f32_e32 v63, v62, v42
	v_mul_f32_e32 v43, v62, v41
	v_fma_f32 v41, v61, v41, -v63
	v_fma_f32 v42, v61, v42, v43
	v_mul_f32_e32 v55, v52, v52
	v_mul_f32_e32 v56, v53, v53
	v_mul_f32_e32 v57, v54, v54
	v_add_f32_dpp v55, v55, v55 quad_perm:[1,0,3,2] row_mask:0xf bank_mask:0xf
	v_add_f32_dpp v56, v56, v56 quad_perm:[1,0,3,2] row_mask:0xf bank_mask:0xf
	v_add_f32_dpp v57, v57, v57 quad_perm:[1,0,3,2] row_mask:0xf bank_mask:0xf
	v_add_f32_dpp v55, v55, v55 quad_perm:[2,3,0,1] row_mask:0xf bank_mask:0xf
	v_add_f32_dpp v56, v56, v56 quad_perm:[2,3,0,1] row_mask:0xf bank_mask:0xf
	v_add_f32_dpp v57, v57, v57 quad_perm:[2,3,0,1] row_mask:0xf bank_mask:0xf
	v_cmp_le_f32_e64 s[28:29], v55, v56
	v_cmp_le_f32_e64 s[30:31], v55, v57
	v_cmp_lt_f32_e32 vcc, v57, v56
	s_and_b64 s[28:29], s[28:29], s[30:31]
	s_andn2_b64 s[30:31], vcc, s[28:29]
	v_cndmask_b32_e64 v44, v52, v53, s[28:29]
	v_cndmask_b32_e64 v45, v54, v53, s[30:31]
	v_cndmask_b32_e64 v46, v40, v41, s[28:29]
	v_cndmask_b32_e64 v47, v42, v41, s[30:31]
	v_mul_f32_e32 v58, v44, v44
	s_nop 1
	v_add_f32_dpp v58, v58, v58 quad_perm:[1,0,3,2] row_mask:0xf bank_mask:0xf
	s_nop 1
	v_add_f32_dpp v58, v58, v58 quad_perm:[2,3,0,1] row_mask:0xf bank_mask:0xf
	v_max_f32_e32 v58, 0x3aa2425, v58
	v_rsq_f32_e32 v58, v58
	s_nop 0
	v_mul_f32_e32 v48, v44, v58
	v_mul_f32_e32 v59, v48, v45
	s_nop 1
	v_add_f32_dpp v59, v59, v59 quad_perm:[1,0,3,2] row_mask:0xf bank_mask:0xf
	s_nop 1
	v_add_f32_dpp v59, v59, v59 quad_perm:[2,3,0,1] row_mask:0xf bank_mask:0xf
	v_fma_f32 v49, -v59, v48, v45
	v_mul_f32_e32 v58, v49, v49
	s_nop 1
	v_add_f32_dpp v58, v58, v58 quad_perm:[1,0,3,2] row_mask:0xf bank_mask:0xf
	s_nop 1
	v_add_f32_dpp v58, v58, v58 quad_perm:[2,3,0,1] row_mask:0xf bank_mask:0xf
	v_max_f32_e32 v58, 0x3aa2425, v58
	v_rsq_f32_e32 v58, v58
	s_nop 0
	v_mul_f32_e32 v50, v49, v58
	v_mov_b32_dpp v43, v47 quad_perm:[2,0,1,3] row_mask:0xf bank_mask:0xf
	v_mov_b32_dpp v63, v47 quad_perm:[1,2,0,3] row_mask:0xf bank_mask:0xf
	v_mov_b32_dpp v62, v50 quad_perm:[2,0,1,3] row_mask:0xf bank_mask:0xf
	v_mov_b32_dpp v61, v50 quad_perm:[1,2,0,3] row_mask:0xf bank_mask:0xf
	v_mul_f32_dpp v60, v46, v43 quad_perm:[1,2,0,3] row_mask:0xf bank_mask:0xf
	v_mul_f32_dpp v51, v48, v62 quad_perm:[1,2,0,3] row_mask:0xf bank_mask:0xf
	s_nop 0
	v_fmac_f32_dpp v60, -v46, v63 quad_perm:[2,0,1,3] row_mask:0xf bank_mask:0xf
	v_fmac_f32_dpp v51, -v48, v61 quad_perm:[2,0,1,3] row_mask:0xf bank_mask:0xf
	v_mul_f32_dpp v52, v46, v48 quad_perm:[0,0,0,0] row_mask:0xf bank_mask:0xf
	v_mul_f32_dpp v53, v46, v48 quad_perm:[1,1,1,1] row_mask:0xf bank_mask:0xf
	v_mul_f32_dpp v54, v46, v48 quad_perm:[2,2,2,2] row_mask:0xf bank_mask:0xf
	v_fmac_f32_dpp v52, v47, v50 quad_perm:[0,0,0,0] row_mask:0xf bank_mask:0xf
	v_fmac_f32_dpp v53, v47, v50 quad_perm:[1,1,1,1] row_mask:0xf bank_mask:0xf
	v_fmac_f32_dpp v54, v47, v50 quad_perm:[2,2,2,2] row_mask:0xf bank_mask:0xf
	v_fmac_f32_dpp v52, v60, v51 quad_perm:[0,0,0,0] row_mask:0xf bank_mask:0xf
	v_fmac_f32_dpp v53, v60, v51 quad_perm:[1,1,1,1] row_mask:0xf bank_mask:0xf
	v_fmac_f32_dpp v54, v60, v51 quad_perm:[2,2,2,2] row_mask:0xf bank_mask:0xf
	v_mov_b32_e32 v55, 0
	v_writelane_b32 v55, s32, 48
	v_writelane_b32 v55, s33, 49
	v_writelane_b32 v55, s34, 50
	v_mul_f32_e32 v55, 0xbc800000, v55
	v_mul_f32_e32 v56, v55, v52
	v_mul_f32_e32 v57, v55, v53
	v_mul_f32_e32 v58, v55, v54
	v_add_f32_dpp v56, v56, v56 quad_perm:[1,0,3,2] row_mask:0xf bank_mask:0xf
	v_add_f32_dpp v57, v57, v57 quad_perm:[1,0,3,2] row_mask:0xf bank_mask:0xf
	v_add_f32_dpp v58, v58, v58 quad_perm:[1,0,3,2] row_mask:0xf bank_mask:0xf
	v_add_f32_dpp v56, v56, v56 quad_perm:[2,3,0,1] row_mask:0xf bank_mask:0xf
	v_add_f32_dpp v57, v57, v57 quad_perm:[2,3,0,1] row_mask:0xf bank_mask:0xf
	v_add_f32_dpp v58, v58, v58 quad_perm:[2,3,0,1] row_mask:0xf bank_mask:0xf
	v_cndmask_b32_e64 v52, v52, v56, s[26:27]
	v_cndmask_b32_e64 v53, v53, v57, s[26:27]
	v_cndmask_b32_e64 v54, v54, v58, s[26:27]
	v_subrev_u32_e32 v59, 48, v0
	v_lshlrev_b32_e32 v59, 4, v59
	s_mov_b32 s20, 0
	s_mov_b32 s21, 0xf0000
	s_mov_b64 exec, s[20:21]
	ds_write_b96 v59, v[52:54] offset:24576
	s_mov_b64 exec, -1
	s_waitcnt lgkmcnt(0)
	s_branch .Ljoin
.Lbulk_waves:
	s_mov_b32 m0, s18
	s_nop 0
	global_load_lds_dwordx4 v1, s[40:41] nt
	global_load_lds_dwordx4 v1, s[40:41] offset:1024 nt
	global_load_lds_dwordx4 v1, s[40:41] offset:2048 nt
	global_load_lds_dwordx4 v1, s[40:41] offset:3072 nt
	s_add_u32 m0, s18, 0x1000
	s_nop 0
	global_load_lds_dwordx4 v1, s[42:43] nt
	s_and_saveexec_b64 s[16:17], s[14:15]
	global_load_lds_dwordx4 v1, s[42:43] offset:1024 nt
	s_mov_b64 exec, s[16:17]
	s_waitcnt vmcnt(0)
	s_waitcnt lgkmcnt(0)
	s_barrier
	ds_read2_b32 v[8:9], v3 offset0:0 offset1:1
	ds_read_b32 v24, v3 offset:8
	ds_read2_b32 v[10:11], v3 offset0:192 offset1:193
	ds_read_b32 v25, v3 offset:776
	ds_read2_b32 v[12:13], v4 offset0:0 offset1:1
	ds_read_b32 v26, v4 offset:8
.Ljoin:
	s_barrier
	v_mov_b32_e32 v6, 0x6000
	ds_read_b96 v[32:34], v6
	ds_read_b96 v[36:38], v6 offset:16
	ds_read_b96 v[40:42], v6 offset:32
	ds_read_b96 v[44:46], v6 offset:48
	v_add_u32_e32 v56, 0xc00, v3
	v_add_u32_e32 v57, 0x1200, v3
	s_waitcnt lgkmcnt(0)
	v_fma_f32 v60, v8, v32, v44
	v_fma_f32 v61, v8, v33, v45
	v_fma_f32 v62, v8, v34, v46
	v_fmac_f32_e32 v60, v9, v36
	v_fmac_f32_e32 v61, v9, v37
	v_fmac_f32_e32 v62, v9, v38
	v_fmac_f32_e32 v60, v24, v40
	v_fmac_f32_e32 v61, v24, v41
	v_fmac_f32_e32 v62, v24, v42
	ds_write2_b32 v3, v60, v61 offset0:0 offset1:1
	ds_write_b32 v3, v62 offset:8
	ds_read2_b32 v[14:15], v4 offset0:192 offset1:193
	ds_read_b32 v27, v4 offset:776
	v_fma_f32 v35, v10, v32, v44
	v_fma_f32 v39, v10, v33, v45
	v_fma_f32 v43, v10, v34, v46
	v_fmac_f32_e32 v35, v11, v36
	v_fmac_f32_e32 v39, v11, v37
	v_fmac_f32_e32 v43, v11, v38
	v_fmac_f32_e32 v35, v25, v40
	v_fmac_f32_e32 v39, v25, v41
	v_fmac_f32_e32 v43, v25, v42
	ds_write2_b32 v3, v35, v39 offset0:192 offset1:193
	ds_write_b32 v3, v43 offset:776
	ds_read_b128 v[48:51], v2
	ds_read2_b32 v[16:17], v56 offset0:0 offset1:1
	ds_read_b32 v28, v56 offset:8
	v_fma_f32 v60, v12, v32, v44
	v_fma_f32 v61, v12, v33, v45
	v_fma_f32 v62, v12, v34, v46
	v_fmac_f32_e32 v60, v13, v36
	v_fmac_f32_e32 v61, v13, v37
	v_fmac_f32_e32 v62, v13, v38
	v_fmac_f32_e32 v60, v26, v40
	v_fmac_f32_e32 v61, v26, v41
	v_fmac_f32_e32 v62, v26, v42
	ds_write2_b32 v4, v60, v61 offset0:0 offset1:1
	ds_write_b32 v4, v62 offset:8
	s_waitcnt lgkmcnt(4)
	global_store_dwordx4 v1, v[48:51], s[10:11] offset:-2048 sc1 nt
	ds_read_b128 v[52:55], v2 offset:1024
	ds_read2_b32 v[18:19], v56 offset0:192 offset1:193
	ds_read_b32 v29, v56 offset:776
	v_fma_f32 v35, v14, v32, v44
	v_fma_f32 v39, v14, v33, v45
	v_fma_f32 v43, v14, v34, v46
	v_fmac_f32_e32 v35, v15, v36
	v_fmac_f32_e32 v39, v15, v37
	v_fmac_f32_e32 v43, v15, v38
	v_fmac_f32_e32 v35, v27, v40
	v_fmac_f32_e32 v39, v27, v41
	v_fmac_f32_e32 v43, v27, v42
	ds_write2_b32 v4, v35, v39 offset0:192 offset1:193
	ds_write_b32 v4, v43 offset:776
	s_waitcnt lgkmcnt(4)
	global_store_dwordx4 v1, v[52:55], s[10:11] offset:-1024 sc1 nt
	ds_read_b128 v[48:51], v2 offset:2048
	ds_read2_b32 v[20:21], v57 offset0:0 offset1:1
	ds_read_b32 v30, v57 offset:8
	v_fma_f32 v60, v16, v32, v44
	v_fma_f32 v61, v16, v33, v45
	v_fma_f32 v62, v16, v34, v46
	v_fmac_f32_e32 v60, v17, v36
	v_fmac_f32_e32 v61, v17, v37
	v_fmac_f32_e32 v62, v17, v38
	v_fmac_f32_e32 v60, v28, v40
	v_fmac_f32_e32 v61, v28, v41
	v_fmac_f32_e32 v62, v28, v42
	ds_write2_b32 v56, v60, v61 offset0:0 offset1:1
	ds_write_b32 v56, v62 offset:8
	s_waitcnt lgkmcnt(4)
	global_store_dwordx4 v1, v[48:51], s[10:11] offset:0 sc1 nt
	ds_read2_b32 v[22:23], v57 offset0:192 offset1:193
	ds_read_b32 v31, v57 offset:776
	v_fma_f32 v35, v18, v32, v44
	v_fma_f32 v39, v18, v33, v45
	v_fma_f32 v43, v18, v34, v46
	v_fmac_f32_e32 v35, v19, v36
	v_fmac_f32_e32 v39, v19, v37
	v_fmac_f32_e32 v43, v19, v38
	v_fmac_f32_e32 v35, v29, v40
	v_fmac_f32_e32 v39, v29, v41
	v_fmac_f32_e32 v43, v29, v42
	ds_write2_b32 v56, v35, v39 offset0:192 offset1:193
	ds_write_b32 v56, v43 offset:776
	ds_read_b128 v[52:55], v2 offset:3072
	s_waitcnt lgkmcnt(7)
	v_fma_f32 v60, v20, v32, v44
	v_fma_f32 v61, v20, v33, v45
	v_fma_f32 v62, v20, v34, v46
	v_fmac_f32_e32 v60, v21, v36
	v_fmac_f32_e32 v61, v21, v37
	v_fmac_f32_e32 v62, v21, v38
	v_fmac_f32_e32 v60, v30, v40
	v_fmac_f32_e32 v61, v30, v41
	v_fmac_f32_e32 v62, v30, v42
	ds_write2_b32 v57, v60, v61 offset0:0 offset1:1
	ds_write_b32 v57, v62 offset:8
	s_waitcnt lgkmcnt(2)
	global_store_dwordx4 v1, v[52:55], s[10:11] offset:1024 sc1 nt
	ds_read_b128 v[48:51], v2 offset:4096
	v_fma_f32 v35, v22, v32, v44
	v_fma_f32 v39, v22, v33, v45
	v_fma_f32 v43, v22, v34, v46
	v_fmac_f32_e32 v35, v23, v36
	v_fmac_f32_e32 v39, v23, v37
	v_fmac_f32_e32 v43, v23, v38
	v_fmac_f32_e32 v35, v31, v40
	v_fmac_f32_e32 v39, v31, v41
	v_fmac_f32_e32 v43, v31, v42
	ds_write2_b32 v57, v35, v39 offset0:192 offset1:193
	ds_write_b32 v57, v43 offset:776
	s_waitcnt lgkmcnt(2)
	global_store_dwordx4 v1, v[48:51], s[10:11] offset:2048 sc1 nt
	ds_read_b128 v[52:55], v2 offset:5120
	s_waitcnt lgkmcnt(0)
	s_and_saveexec_b64 s[16:17], s[14:15]
	global_store_dwordx4 v1, v[52:55], s[10:11] offset:3072 sc1 nt
	s_endpgm
